# speedup vs baseline: 1.0292x; 1.0051x over previous
_Z8dog_mainPKfS0_S0_S0_S0_S0_S0_Pf:
	s_load_dwordx8 s[12:19], s[0:1], 0x0
	s_load_dwordx8 s[20:27], s[0:1], 0x20
	s_and_b32 s3, s2, 7
	s_lshl_b32 s3, s3, 5
	s_lshr_b32 s4, s2, 3
	s_add_i32 s4, s3, s4
	s_lshl_b32 s8, s4, 18
	v_and_b32_e32 v1, 63, v0
	v_lshrrev_b32_e32 v2, 6, v0
	v_and_b32_e32 v7, 31, v0
	v_lshlrev_b32_e32 v6, 4, v1
	v_lshl_or_b32 v5, v2, 5, v7
	v_lshl_or_b32 v6, v2, 12, v6
	v_lshlrev_b32_e32 v5, 2, v5
	s_waitcnt lgkmcnt(0)
	s_add_u32 s12, s12, s8
	s_addc_u32 s13, s13, 0
	global_load_dwordx4 v[128:131], v6, s[12:13] offset:0 nt
	global_load_dwordx4 v[132:135], v6, s[12:13] offset:1024 nt
	global_load_dwordx4 v[136:139], v6, s[12:13] offset:2048 nt
	global_load_dwordx4 v[140:143], v6, s[12:13] offset:3072 nt
	global_load_dword v32, v5, s[18:19]
	global_load_dword v33, v5, s[20:21]
	global_load_dword v34, v5, s[22:23]
	global_load_dword v35, v5, s[24:25]
	global_load_dword v36, v5, s[14:15]
	global_load_dword v37, v5, s[16:17]
	v_add_u32_e32 v6, 0x8000, v6
	global_load_dwordx4 v[144:147], v6, s[12:13] offset:0 nt
	global_load_dwordx4 v[148:151], v6, s[12:13] offset:1024 nt
	global_load_dwordx4 v[152:155], v6, s[12:13] offset:2048 nt
	global_load_dwordx4 v[156:159], v6, s[12:13] offset:3072 nt
	s_and_b32 s6, s4, 3
	s_lshr_b32 s7, s4, 2
	v_and_b32_e32 v3, 15, v0
	v_bfe_u32 v7, v0, 4, 2
	v_and_b32_e32 v16, 1, v0
	v_cmp_eq_u32_e64 s[30:31], 0, v16
	v_and_b32_e32 v17, 2, v0
	v_cmp_eq_u32_e64 s[32:33], 0, v17
	v_and_b32_e32 v16, 3, v0
	v_lshrrev_b32_e32 v17, 2, v1
	v_lshlrev_b32_e32 v16, 5, v16
	v_lshl_add_u32 v16, v17, 1, v16
	v_lshrrev_b32_e32 v17, 1, v2
	s_movk_i32 s10, 0x110
	v_mad_u32_u24 v16, v17, s10, v16
	v_and_b32_e32 v17, 1, v2
	v_lshl_add_u32 v14, v17, 7, v16
	v_lshlrev_b32_e32 v17, 4, v7
	v_mad_u32_u24 v15, v3, s10, v17
	s_lshl_b32 s11, s6, 5
	v_lshl_add_u32 v18, v7, 2, s11
	v_cvt_f32_u32_e32 v18, v18
	v_lshlrev_b32_e32 v19, 3, v7
	v_cvt_f32_u32_e32 v19, v19
	s_waitcnt vmcnt(4)
	v_lshlrev_b32_e32 v16, 2, v3
	v_add_u32_e32 v17, 64, v16
	ds_bpermute_b32 v40, v16, v32
	ds_bpermute_b32 v46, v17, v32
	ds_bpermute_b32 v41, v16, v33
	ds_bpermute_b32 v47, v17, v33
	ds_bpermute_b32 v42, v16, v34
	ds_bpermute_b32 v48, v17, v34
	ds_bpermute_b32 v43, v16, v35
	ds_bpermute_b32 v49, v17, v35
	ds_bpermute_b32 v44, v16, v36
	ds_bpermute_b32 v50, v17, v36
	ds_bpermute_b32 v45, v16, v37
	ds_bpermute_b32 v51, v17, v37
	s_waitcnt lgkmcnt(0)
	v_add_f32_e32 v41, v40, v41
	v_sub_f32_e32 v12, v19, v42
	v_sub_f32_e32 v13, v18, v43
	v_rcp_f32_e32 v42, v40
	v_rcp_f32_e32 v43, v41
	s_nop 0
	v_fma_f32 v20, -v40, v42, 1.0
	v_fma_f32 v42, v20, v42, v42
	v_fma_f32 v20, -v41, v43, 1.0
	v_fma_f32 v43, v20, v43, v43
	v_mul_f32_e32 v8, 0xbf38aa3b, v42
	v_mul_f32_e32 v9, 0xbf38aa3b, v43
	v_mul_f32_e32 v44, v44, v42
	v_mul_f32_e32 v45, v45, v43
	v_mul_f32_e32 v10, 0x3e22f983, v44
	v_mul_f32_e32 v11, 0x3e22f983, v45
	v_add_f32_e32 v47, v46, v47
	v_sub_f32_e32 v2, v19, v48
	v_sub_f32_e32 v3, v18, v49
	v_rcp_f32_e32 v48, v46
	v_rcp_f32_e32 v49, v47
	s_nop 0
	v_fma_f32 v20, -v46, v48, 1.0
	v_fma_f32 v48, v20, v48, v48
	v_fma_f32 v20, -v47, v49, 1.0
	v_fma_f32 v49, v20, v49, v49
	v_mul_f32_e32 v28, 0xbf38aa3b, v48
	v_mul_f32_e32 v29, 0xbf38aa3b, v49
	v_mul_f32_e32 v50, v50, v48
	v_mul_f32_e32 v51, v51, v49
	v_mul_f32_e32 v30, 0x3e22f983, v50
	v_mul_f32_e32 v31, 0x3e22f983, v51
	s_getpc_b64 s[44:45]
